# speedup vs baseline: 1.0185x; 1.0101x over previous
.Lhold_done:
	v_cmp_ne_u32_e64 s[28:29], 0, v12
	v_cmp_ne_u32_e64 s[30:31], 0, v13
	v_cmp_ne_u32_e64 s[32:33], 0, v14
	v_cmp_ne_u32_e64 s[34:35], 0, v15
	v_cmp_ne_u32_e64 s[36:37], 0, v16
	v_cmp_ne_u32_e64 s[38:39], 0, v17
	v_cmp_ne_u32_e64 s[40:41], 0, v18
	v_cmp_ne_u32_e64 s[42:43], 0, v19
	s_lshl_b32 s3, s15, 9
	v_lshlrev_b32_e32 v20, 2, v10
	v_mbcnt_lo_u32_b32 v8, s28, 0
	v_mbcnt_hi_u32_b32 v8, s29, v8
	v_add_lshl_u32 v9, v8, s3, 1
	s_mov_b64 exec, s[28:29]
	ds_write_b16 v9, v20
	s_mov_b64 exec, -1
	s_bcnt1_i32_b64 s4, s[28:29]
	s_add_u32 s3, s3, s4
	v_mbcnt_lo_u32_b32 v8, s30, 0
	v_mbcnt_hi_u32_b32 v8, s31, v8
	v_add_lshl_u32 v9, v8, s3, 1
	v_add_u32_e32 v21, 1, v20
	s_mov_b64 exec, s[30:31]
	ds_write_b16 v9, v21
	s_mov_b64 exec, -1
	s_bcnt1_i32_b64 s4, s[30:31]
	s_add_u32 s3, s3, s4
	v_mbcnt_lo_u32_b32 v8, s32, 0
	v_mbcnt_hi_u32_b32 v8, s33, v8
	v_add_lshl_u32 v9, v8, s3, 1
	v_add_u32_e32 v21, 2, v20
	s_mov_b64 exec, s[32:33]
	ds_write_b16 v9, v21
	s_mov_b64 exec, -1
	s_bcnt1_i32_b64 s4, s[32:33]
	s_add_u32 s3, s3, s4
	v_mbcnt_lo_u32_b32 v8, s34, 0
	v_mbcnt_hi_u32_b32 v8, s35, v8
	v_add_lshl_u32 v9, v8, s3, 1
	v_add_u32_e32 v21, 3, v20
	s_mov_b64 exec, s[34:35]
	ds_write_b16 v9, v21
	s_mov_b64 exec, -1
	s_bcnt1_i32_b64 s4, s[34:35]
	s_add_u32 s3, s3, s4
	v_mbcnt_lo_u32_b32 v8, s36, 0
	v_mbcnt_hi_u32_b32 v8, s37, v8
	v_add_lshl_u32 v9, v8, s3, 1
	v_add_u32_e32 v21, 0x100, v20
	s_mov_b64 exec, s[36:37]
	ds_write_b16 v9, v21
	s_mov_b64 exec, -1
	s_bcnt1_i32_b64 s4, s[36:37]
	s_add_u32 s3, s3, s4
	v_mbcnt_lo_u32_b32 v8, s38, 0
	v_mbcnt_hi_u32_b32 v8, s39, v8
	v_add_lshl_u32 v9, v8, s3, 1
	v_add_u32_e32 v21, 0x101, v20
	s_mov_b64 exec, s[38:39]
	ds_write_b16 v9, v21
	s_mov_b64 exec, -1
	s_bcnt1_i32_b64 s4, s[38:39]
	s_add_u32 s3, s3, s4
	v_mbcnt_lo_u32_b32 v8, s40, 0
	v_mbcnt_hi_u32_b32 v8, s41, v8
	v_add_lshl_u32 v9, v8, s3, 1
	v_add_u32_e32 v21, 0x102, v20
	s_mov_b64 exec, s[40:41]
	ds_write_b16 v9, v21
	s_mov_b64 exec, -1
	s_bcnt1_i32_b64 s4, s[40:41]
	s_add_u32 s3, s3, s4
	v_mbcnt_lo_u32_b32 v8, s42, 0
	v_mbcnt_hi_u32_b32 v8, s43, v8
	v_add_lshl_u32 v9, v8, s3, 1
	v_add_u32_e32 v21, 0x103, v20
	s_mov_b64 exec, s[42:43]
	ds_write_b16 v9, v21
	s_mov_b64 exec, -1
	s_bcnt1_i32_b64 s4, s[42:43]
	s_add_u32 s3, s3, s4
	s_lshl_b32 s4, s15, 9
	s_sub_u32 s3, s3, s4
	s_and_saveexec_b64 s[0:1], vcc
	ds_write_b128 v11, v[2:5] offset:16384
	s_or_b64 exec, exec, s[0:1]
	v_cmp_gt_i32_e32 vcc, s3, v10
	v_mov_b32_e32 v2, 0
	s_waitcnt lgkmcnt(0)
	s_and_saveexec_b64 s[0:1], vcc
	s_cbranch_execz .Lmid_bar
	v_lshlrev_b32_e32 v3, 1, v10
	v_lshl_or_b32 v3, v1, 10, v3
	v_mov_b32_e32 v4, v10
	ds_read_u16 v5, v3
	s_waitcnt lgkmcnt(0)
	v_add_u32_e32 v8, v6, v5
	v_lshlrev_b32_e32 v8, 4, v8
	global_load_dwordx4 v[12:15], v8, s[16:17] nt
	global_load_dwordx4 v[16:19], v8, s[18:19] nt
	v_lshlrev_b32_e32 v5, 4, v5

	.amdhsa_kernel _Z12giou_partialPK15HIP_vector_typeIfLj4EES2_S2_PKiPS_IfLj2EE
		.amdhsa_group_segment_fixed_size 24704
		.amdhsa_private_segment_fixed_size 0
		.amdhsa_kernarg_size 40
		.amdhsa_user_sgpr_count 2
		.amdhsa_user_sgpr_dispatch_ptr 0
		.amdhsa_user_sgpr_queue_ptr 0
		.amdhsa_user_sgpr_kernarg_segment_ptr 1
		.amdhsa_user_sgpr_dispatch_id 0
		.amdhsa_user_sgpr_kernarg_preload_length 0
		.amdhsa_user_sgpr_kernarg_preload_offset 0
		.amdhsa_user_sgpr_private_segment_size 0
		.amdhsa_uses_dynamic_stack 0
		.amdhsa_enable_private_segment 0
		.amdhsa_system_sgpr_workgroup_id_x 1
		.amdhsa_system_sgpr_workgroup_id_y 0
		.amdhsa_system_sgpr_workgroup_id_z 0
		.amdhsa_system_sgpr_workgroup_info 0
		.amdhsa_system_vgpr_workitem_id 0
		.amdhsa_next_free_vgpr 26
		.amdhsa_next_free_sgpr 44
		.amdhsa_accum_offset 28
		.amdhsa_reserve_vcc 1
		.amdhsa_float_round_mode_32 0
		.amdhsa_float_round_mode_16_64 0
		.amdhsa_float_denorm_mode_32 3
		.amdhsa_float_denorm_mode_16_64 3
		.amdhsa_dx10_clamp 1
		.amdhsa_ieee_mode 1
		.amdhsa_fp16_overflow 0
		.amdhsa_tg_split 0
		.amdhsa_exception_fp_ieee_invalid_op 0
		.amdhsa_exception_fp_denorm_src 0
		.amdhsa_exception_fp_ieee_div_zero 0
		.amdhsa_exception_fp_ieee_overflow 0
		.amdhsa_exception_fp_ieee_underflow 0
		.amdhsa_exception_fp_ieee_inexact 0
		.amdhsa_exception_int_div_zero 0
	.end_amdhsa_kernel

.Lfunc_end0:
	.size	_Z12giou_partialPK15HIP_vector_typeIfLj4EES2_S2_PKiPS_IfLj2EE, .Lfunc_end0-_Z12giou_partialPK15HIP_vector_typeIfLj4EES2_S2_PKiPS_IfLj2EE
	.set _Z12giou_partialPK15HIP_vector_typeIfLj4EES2_S2_PKiPS_IfLj2EE.num_vgpr, 26
	.set _Z12giou_partialPK15HIP_vector_typeIfLj4EES2_S2_PKiPS_IfLj2EE.num_agpr, 0
	.set _Z12giou_partialPK15HIP_vector_typeIfLj4EES2_S2_PKiPS_IfLj2EE.numbered_sgpr, 44
	.set _Z12giou_partialPK15HIP_vector_typeIfLj4EES2_S2_PKiPS_IfLj2EE.num_named_barrier, 0
	.set _Z12giou_partialPK15HIP_vector_typeIfLj4EES2_S2_PKiPS_IfLj2EE.private_seg_size, 0
	.set _Z12giou_partialPK15HIP_vector_typeIfLj4EES2_S2_PKiPS_IfLj2EE.uses_vcc, 1
	.set _Z12giou_partialPK15HIP_vector_typeIfLj4EES2_S2_PKiPS_IfLj2EE.uses_flat_scratch, 0
	.set _Z12giou_partialPK15HIP_vector_typeIfLj4EES2_S2_PKiPS_IfLj2EE.has_dyn_sized_stack, 0
	.set _Z12giou_partialPK15HIP_vector_typeIfLj4EES2_S2_PKiPS_IfLj2EE.has_recursion, 0
	.set _Z12giou_partialPK15HIP_vector_typeIfLj4EES2_S2_PKiPS_IfLj2EE.has_indirect_call, 0

amdhsa.kernels:
  - .agpr_count:     0
    .args:
      - .actual_access:  read_only
        .address_space:  global
        .offset:         0
        .size:           8
        .value_kind:     global_buffer
      - .actual_access:  read_only
        .address_space:  global
        .offset:         8
        .size:           8
        .value_kind:     global_buffer
      - .actual_access:  read_only
        .address_space:  global
        .offset:         16
        .size:           8
        .value_kind:     global_buffer
      - .actual_access:  read_only
        .address_space:  global
        .offset:         24
        .size:           8
        .value_kind:     global_buffer
      - .actual_access:  write_only
        .address_space:  global
        .offset:         32
        .size:           8
        .value_kind:     global_buffer
    .group_segment_fixed_size: 24704
    .kernarg_segment_align: 8
    .kernarg_segment_size: 40
    .language:       OpenCL C
    .language_version:
      - 2
      - 0
    .max_flat_workgroup_size: 1024
    .name:           _Z12giou_partialPK15HIP_vector_typeIfLj4EES2_S2_PKiPS_IfLj2EE
    .private_segment_fixed_size: 0
    .sgpr_count:     50
    .sgpr_spill_count: 0
    .symbol:         _Z12giou_partialPK15HIP_vector_typeIfLj4EES2_S2_PKiPS_IfLj2EE.kd
    .uniform_work_group_size: 1
    .uses_dynamic_stack: false
    .vgpr_count:     26
    .vgpr_spill_count: 0
    .wavefront_size: 64
  - .agpr_count:     0
    .args:
      - .actual_access:  read_only
        .address_space:  global
        .offset:         0
        .size:           8
        .value_kind:     global_buffer
      - .actual_access:  write_only
        .address_space:  global
        .offset:         8
        .size:           8
        .value_kind:     global_buffer
    .group_segment_fixed_size: 0
    .kernarg_segment_align: 8
    .kernarg_segment_size: 16
    .language:       OpenCL C
    .language_version:
      - 2
      - 0
    .max_flat_workgroup_size: 64
    .name:           _Z10giou_finalPK15HIP_vector_typeIfLj2EEPf
    .private_segment_fixed_size: 0
    .sgpr_count:     18
    .sgpr_spill_count: 0
    .symbol:         _Z10giou_finalPK15HIP_vector_typeIfLj2EEPf.kd
    .uniform_work_group_size: 1
    .uses_dynamic_stack: false
    .vgpr_count:     18
    .vgpr_spill_count: 0
    .wavefront_size: 64
